# attention main loop: softmax row sums by one 16x16x128 fp8 MFMA (32 cyc) against a constant ones-pattern A operand instead of the 32x32x64 ones-block MFMA (64 cyc) + 2 LDS reads; same fp8 MFMA kind, f
# speedup vs baseline: 1.0123x; 1.0076x over previous
.LBB0_424:
	s_mov_b32 s14, s47
	v_mbcnt_lo_u32_b32 v1, -1, 0
	v_mbcnt_hi_u32_b32 v1, -1, v1
	v_and_b32_e32 v252, 31, v1
	v_mov_b32_e32 v253, 0x38383838
	v_cmp_eq_u32_e32 vcc, 0, v252
	s_nop 1
	v_cndmask_b32_e32 v240, 0, v253, vcc
	v_cmp_eq_u32_e32 vcc, 17, v252
	s_nop 1
	v_cndmask_b32_e32 v241, 0, v253, vcc
	v_or_b32_e32 v240, v240, v241
	v_mov_b32_e32 v241, v240
	v_mov_b32_e32 v242, v240
	v_mov_b32_e32 v243, v240
	v_mov_b32_e32 v244, v240
	v_mov_b32_e32 v245, v240
	v_mov_b32_e32 v246, v240
	v_mov_b32_e32 v247, v240
	v_mov_b32_e32 v248, 0
	v_mov_b32_e32 v249, 0
	v_mov_b32_e32 v250, 0
	v_mov_b32_e32 v251, 0
	s_lshl_b32 s3, s2, 7
	v_lshl_add_u32 v5, s14, 6, v1
	v_ashrrev_i32_e32 v10, 6, v5
	v_lshlrev_b32_e32 v6, 5, v10
	v_and_b32_e32 v2, 31, v1
	v_and_b32_e32 v6, 0x60, v6
	v_add3_u32 v6, v2, s16, v6
	v_ashrrev_i32_e32 v7, 31, v6
	v_ashrrev_i32_e32 v3, 8, v5
	v_lshlrev_b64 v[6:7], 10, v[6:7]
	v_lshl_add_u64 v[6:7], s[80:81], 0, v[6:7]
	s_and_b32 s24, s3, 0x180
	v_lshlrev_b32_e32 v8, 6, v3
	v_bfe_u32 v4, v1, 5, 1
	v_lshl_add_u64 v[6:7], v[6:7], 0, s[24:25]
	v_ashrrev_i32_e32 v9, 31, v8
	v_lshl_add_u64 v[6:7], v[6:7], 0, v[8:9]
	v_lshlrev_b32_e32 v8, 5, v4
	v_mov_b32_e32 v9, v0
	v_mov_b32_e32 v207, 0x7f7f7f7f
	v_mov_b32_e32 v218, 0x72727272
	v_mov_b32_e32 v96, 0x3ac00000
	v_mov_b32_e32 v97, 0x3ac00000
	v_mov_b32_e32 v98, 0x3ac00000
	v_mov_b32_e32 v99, 0x3ac00000
	v_mov_b32_e32 v100, 0x3ac00000
	v_mov_b32_e32 v101, 0x3ac00000
	v_mov_b32_e32 v102, 0x3ac00000
	v_mov_b32_e32 v103, 0x3ac00000
	v_mov_b32_e32 v104, 0x3ac00000
	v_mov_b32_e32 v105, 0x3ac00000
	v_mov_b32_e32 v106, 0x3ac00000
	v_mov_b32_e32 v107, 0x3ac00000
	v_mov_b32_e32 v108, 0x3ac00000
	v_mov_b32_e32 v109, 0x3ac00000
	v_mov_b32_e32 v110, 0x3ac00000
	v_mov_b32_e32 v111, 0x3ac00000
	v_lshl_add_u64 v[6:7], v[6:7], 0, v[8:9]
	global_load_dwordx4 v[196:199], v[6:7], off offset:16
	global_load_dwordx4 v[192:195], v[6:7], off
	v_readfirstlane_b32 s3, v10
	s_mov_b32 s4, 0x38383838
	v_cmp_gt_i32_e32 vcc, s57, v5
	s_and_saveexec_b64 s[22:23], vcc
	s_cbranch_execz .LBB0_427
	s_mov_b32 s6, s4
	s_mov_b32 s7, s4
	s_mov_b32 s5, s4
	v_lshlrev_b32_e32 v6, 4, v1
	v_mov_b64_e32 v[10:11], s[6:7]
	v_lshl_add_u32 v6, s14, 10, v6
	s_mov_b64 s[84:85], 0
	v_mov_b64_e32 v[8:9], s[4:5]
	v_mov_b32_e32 v7, v5

.LBB0_430:
	s_waitcnt lgkmcnt(0)
	v_mfma_scale_f32_32x32x64_f8f6f4 v[144:159], v[184:191], v[192:199], v[96:111], v207, v218 op_sel_hi:[0,0,0]
	ds_read_b128 v[2:5], v221
	ds_read_b128 v[184:187], v221 offset:2048
	ds_read_b128 v[6:9], v222
	ds_read_b128 v[168:171], v221 offset:4096
	ds_read_b128 v[188:191], v222 offset:2048
	ds_read_b128 v[172:175], v222 offset:4096
	v_cvt_pknorm_u16_f32 v1, v112, v113
	v_cvt_pknorm_u16_f32 v10, v114, v115
	v_perm_b32 v160, v10, v1, s55
	v_cvt_pknorm_u16_f32 v1, v116, v117
	v_cvt_pknorm_u16_f32 v10, v118, v119
	v_perm_b32 v161, v10, v1, s55
	v_cvt_pknorm_u16_f32 v1, v120, v121
	v_cvt_pknorm_u16_f32 v10, v122, v123
	v_perm_b32 v162, v10, v1, s55
	v_cvt_pknorm_u16_f32 v1, v124, v125
	v_cvt_pknorm_u16_f32 v10, v126, v127
	v_perm_b32 v163, v10, v1, s55
	s_waitcnt lgkmcnt(6)
	v_mfma_scale_f32_32x32x64_f8f6f4 v[112:127], v[176:183], v[192:199], v[96:111], v207, v218 op_sel_hi:[0,0,0]
	s_add_u32 s52, s4, s84
	s_addc_u32 s54, s5, s85
	s_add_u32 s14, s52, 0xa000
	s_addc_u32 s15, s54, 0
	v_cvt_pknorm_u16_f32 v1, v128, v129
	v_cvt_pknorm_u16_f32 v10, v130, v131
	s_add_u32 s56, s6, s84
	v_perm_b32 v164, v10, v1, s55
	v_cvt_pknorm_u16_f32 v1, v132, v133
	v_cvt_pknorm_u16_f32 v10, v134, v135
	s_addc_u32 s61, s7, s85
	v_perm_b32 v165, v10, v1, s55
	v_cvt_pknorm_u16_f32 v1, v136, v137
	v_cvt_pknorm_u16_f32 v10, v138, v139
	s_add_u32 s20, s56, 0xa000
	v_perm_b32 v166, v10, v1, s55
	v_cvt_pknorm_u16_f32 v1, v140, v141
	v_cvt_pknorm_u16_f32 v10, v142, v143
	s_addc_u32 s21, s61, 0
	v_perm_b32 v167, v10, v1, s55
	s_mov_b32 m0, s45
	v_lshl_add_u64 v[10:11], s[14:15], 0, v[200:201]
	global_load_lds_dwordx4 v[10:11], off
	v_lshl_add_u64 v[10:11], s[20:21], 0, v[202:203]
	s_add_i32 m0, s23, 0xc800
	s_nop 0
	global_load_lds_dwordx4 v[10:11], off
	s_waitcnt lgkmcnt(0)
	v_mfma_scale_f32_32x32x64_f8f6f4 v[64:79], v[2:9], v[160:167], v[64:79], v207, v207 op_sel_hi:[0,0,0]
	ds_read_b128 v[136:139], v221 offset:6144
	ds_read_b128 v[140:143], v222 offset:6144
	v_mfma_scale_f32_32x32x64_f8f6f4 v[48:63], v[184:191], v[160:167], v[48:63], v207, v207 op_sel_hi:[0,0,0]
	ds_read_b128 v[128:131], v219 offset:16384
	ds_read_b128 v[2:5], v219 offset:20480
	ds_read_b128 v[132:135], v220 offset:16384
	ds_read_b128 v[6:9], v220 offset:20480
	v_mov_b32_e32 v1, v144
	v_max3_f32 v1, v1, v144, v145
	v_max3_f32 v1, v1, v146, v147
	v_max3_f32 v1, v1, v148, v149
	v_max3_f32 v1, v1, v150, v151
	v_max3_f32 v1, v1, v152, v153
	v_max3_f32 v1, v1, v154, v155
	v_max3_f32 v1, v1, v156, v157
	v_max3_f32 v1, v1, v158, v159
	v_mfma_scale_f32_32x32x64_f8f6f4 v[32:47], v[168:175], v[160:167], v[32:47], v207, v207 op_sel_hi:[0,0,0]
	v_max3_f32 v1, v1, v112, v113
	v_max3_f32 v1, v1, v114, v115
	v_max3_f32 v1, v1, v116, v117
	v_max3_f32 v1, v1, v118, v119
	v_max3_f32 v1, v1, v120, v121
	v_max3_f32 v1, v1, v122, v123
	v_max3_f32 v1, v1, v124, v125
	v_max3_f32 v1, v1, v126, v127
	v_cmp_ge_f32_e32 vcc, s53, v1
	s_cmp_eq_u64 vcc, exec
	s_waitcnt lgkmcnt(0)
	v_mfma_scale_f32_32x32x64_f8f6f4 v[16:31], v[136:143], v[160:167], v[16:31], v207, v207 op_sel_hi:[0,0,0]
	v_mfma_scale_f32_16x16x128_f8f6f4 v[248:251], v[240:247], v[160:167], v[248:251], v207, v207 op_sel_hi:[0,0,0]
	s_cbranch_scc0 .LBB0_438
.LBB0_431:
	s_waitcnt vmcnt(4)
	s_waitcnt lgkmcnt(0)
	s_barrier
	v_mfma_scale_f32_32x32x64_f8f6f4 v[160:175], v[128:135], v[192:199], v[96:111], v207, v218 op_sel_hi:[0,0,0]
	ds_read_b128 v[224:227], v221 offset:10240
	ds_read_b128 v[232:235], v221 offset:12288
	ds_read_b128 v[228:231], v222 offset:10240
	ds_read_b128 v[136:139], v221 offset:14336
	ds_read_b128 v[236:239], v222 offset:12288
	ds_read_b128 v[140:143], v222 offset:14336
	v_cvt_pknorm_u16_f32 v1, v144, v145
	v_cvt_pknorm_u16_f32 v10, v146, v147
	v_perm_b32 v128, v10, v1, s55
	v_cvt_pknorm_u16_f32 v1, v148, v149
	v_cvt_pknorm_u16_f32 v10, v150, v151
	v_perm_b32 v129, v10, v1, s55
	v_cvt_pknorm_u16_f32 v1, v152, v153
	v_cvt_pknorm_u16_f32 v10, v154, v155
	v_perm_b32 v130, v10, v1, s55
	v_cvt_pknorm_u16_f32 v1, v156, v157
	v_cvt_pknorm_u16_f32 v10, v158, v159
	v_perm_b32 v131, v10, v1, s55
	v_mfma_scale_f32_32x32x64_f8f6f4 v[176:191], v[2:9], v[192:199], v[96:111], v207, v218 op_sel_hi:[0,0,0]
	v_cvt_pknorm_u16_f32 v1, v112, v113
	v_cvt_pknorm_u16_f32 v2, v114, v115
	s_add_u32 s14, s52, 0xc000
	v_perm_b32 v132, v2, v1, s55
	v_cvt_pknorm_u16_f32 v1, v116, v117
	v_cvt_pknorm_u16_f32 v2, v118, v119
	s_addc_u32 s15, s54, 0
	v_perm_b32 v133, v2, v1, s55
	v_cvt_pknorm_u16_f32 v1, v120, v121
	v_cvt_pknorm_u16_f32 v2, v122, v123
	s_add_u32 s20, s56, 0xc000
	v_perm_b32 v134, v2, v1, s55
	v_cvt_pknorm_u16_f32 v1, v124, v125
	v_cvt_pknorm_u16_f32 v2, v126, v127
	s_addc_u32 s21, s61, 0
	v_perm_b32 v135, v2, v1, s55
	s_mov_b32 m0, s59
	v_lshl_add_u64 v[2:3], s[14:15], 0, v[200:201]
	global_load_lds_dwordx4 v[2:3], off
	v_lshl_add_u64 v[2:3], s[20:21], 0, v[202:203]
	s_mov_b32 m0, s23
	s_nop 0
	global_load_lds_dwordx4 v[2:3], off
	s_waitcnt lgkmcnt(0)
	v_mfma_scale_f32_32x32x64_f8f6f4 v[64:79], v[224:231], v[128:135], v[64:79], v207, v207 op_sel_hi:[0,0,0]
	ds_read_b128 v[120:123], v221 offset:16384
	ds_read_b128 v[124:127], v222 offset:16384
	v_mfma_scale_f32_32x32x64_f8f6f4 v[48:63], v[232:239], v[128:135], v[48:63], v207, v207 op_sel_hi:[0,0,0]
	ds_read_b128 v[112:115], v219 offset:24576
	ds_read_b128 v[2:5], v219 offset:28672
	ds_read_b128 v[116:119], v220 offset:24576
	ds_read_b128 v[6:9], v220 offset:28672
	v_mov_b32_e32 v1, v160
	v_max3_f32 v1, v1, v160, v161
	v_max3_f32 v1, v1, v162, v163
	v_max3_f32 v1, v1, v164, v165
	v_max3_f32 v1, v1, v166, v167
	v_max3_f32 v1, v1, v168, v169
	v_max3_f32 v1, v1, v170, v171
	v_max3_f32 v1, v1, v172, v173
	v_max3_f32 v1, v1, v174, v175
	v_mfma_scale_f32_32x32x64_f8f6f4 v[32:47], v[136:143], v[128:135], v[32:47], v207, v207 op_sel_hi:[0,0,0]
	v_max3_f32 v1, v1, v176, v177
	v_max3_f32 v1, v1, v178, v179
	v_max3_f32 v1, v1, v180, v181
	v_max3_f32 v1, v1, v182, v183
	v_max3_f32 v1, v1, v184, v185
	v_max3_f32 v1, v1, v186, v187
	v_max3_f32 v1, v1, v188, v189
	v_max3_f32 v1, v1, v190, v191
	v_cmp_ge_f32_e32 vcc, s53, v1
	s_cmp_eq_u64 vcc, exec
	s_waitcnt lgkmcnt(0)
	v_mfma_scale_f32_32x32x64_f8f6f4 v[16:31], v[120:127], v[128:135], v[16:31], v207, v207 op_sel_hi:[0,0,0]
	v_mfma_scale_f32_16x16x128_f8f6f4 v[248:251], v[240:247], v[128:135], v[248:251], v207, v207 op_sel_hi:[0,0,0]
	s_cbranch_scc0 .LBB0_441
.LBB0_432:
	s_waitcnt vmcnt(4)
	s_waitcnt lgkmcnt(0)
	s_barrier
	v_mfma_scale_f32_32x32x64_f8f6f4 v[128:143], v[112:119], v[192:199], v[96:111], v207, v218 op_sel_hi:[0,0,0]
	ds_read_b128 v[224:227], v221 offset:20480
	ds_read_b128 v[232:235], v221 offset:22528
	ds_read_b128 v[228:231], v222 offset:20480
	ds_read_b128 v[120:123], v221 offset:24576
	ds_read_b128 v[236:239], v222 offset:22528
	ds_read_b128 v[124:127], v222 offset:24576
	v_cvt_pknorm_u16_f32 v1, v160, v161
	v_cvt_pknorm_u16_f32 v10, v162, v163
	v_perm_b32 v112, v10, v1, s55
	v_cvt_pknorm_u16_f32 v1, v164, v165
	v_cvt_pknorm_u16_f32 v10, v166, v167
	v_perm_b32 v113, v10, v1, s55
	v_cvt_pknorm_u16_f32 v1, v168, v169
	v_cvt_pknorm_u16_f32 v10, v170, v171
	v_perm_b32 v114, v10, v1, s55
	v_cvt_pknorm_u16_f32 v1, v172, v173
	v_cvt_pknorm_u16_f32 v10, v174, v175
	v_perm_b32 v115, v10, v1, s55
	v_mfma_scale_f32_32x32x64_f8f6f4 v[144:159], v[2:9], v[192:199], v[96:111], v207, v218 op_sel_hi:[0,0,0]
	v_cvt_pknorm_u16_f32 v1, v176, v177
	v_cvt_pknorm_u16_f32 v2, v178, v179
	s_add_u32 s14, s52, 0xe000
	v_perm_b32 v116, v2, v1, s55
	v_cvt_pknorm_u16_f32 v1, v180, v181
	v_cvt_pknorm_u16_f32 v2, v182, v183
	s_addc_u32 s15, s54, 0
	v_perm_b32 v117, v2, v1, s55
	v_cvt_pknorm_u16_f32 v1, v184, v185
	v_cvt_pknorm_u16_f32 v2, v186, v187
	s_add_u32 s20, s56, 0xe000
	v_perm_b32 v118, v2, v1, s55
	v_cvt_pknorm_u16_f32 v1, v188, v189
	v_cvt_pknorm_u16_f32 v2, v190, v191
	s_addc_u32 s21, s61, 0
	v_perm_b32 v119, v2, v1, s55
	s_mov_b32 m0, s48
	v_lshl_add_u64 v[2:3], s[14:15], 0, v[200:201]
	global_load_lds_dwordx4 v[2:3], off
	v_lshl_add_u64 v[2:3], s[20:21], 0, v[202:203]
	s_mov_b32 m0, s2
	s_nop 0
	global_load_lds_dwordx4 v[2:3], off
	s_waitcnt lgkmcnt(0)
	v_mfma_scale_f32_32x32x64_f8f6f4 v[64:79], v[224:231], v[112:119], v[64:79], v207, v207 op_sel_hi:[0,0,0]
	ds_read_b128 v[168:171], v221 offset:26624
	ds_read_b128 v[172:175], v222 offset:26624
	v_mfma_scale_f32_32x32x64_f8f6f4 v[48:63], v[232:239], v[112:119], v[48:63], v207, v207 op_sel_hi:[0,0,0]
	ds_read_b128 v[160:163], v219 offset:32768
	ds_read_b128 v[2:5], v219 offset:36864
	ds_read_b128 v[164:167], v220 offset:32768
	ds_read_b128 v[6:9], v220 offset:36864
	v_mov_b32_e32 v1, v128
	v_max3_f32 v1, v1, v128, v129
	v_max3_f32 v1, v1, v130, v131
	v_max3_f32 v1, v1, v132, v133
	v_max3_f32 v1, v1, v134, v135
	v_max3_f32 v1, v1, v136, v137
	v_max3_f32 v1, v1, v138, v139
	v_max3_f32 v1, v1, v140, v141
	v_max3_f32 v1, v1, v142, v143
	v_mfma_scale_f32_32x32x64_f8f6f4 v[32:47], v[120:127], v[112:119], v[32:47], v207, v207 op_sel_hi:[0,0,0]
	v_max3_f32 v1, v1, v144, v145
	v_max3_f32 v1, v1, v146, v147
	v_max3_f32 v1, v1, v148, v149
	v_max3_f32 v1, v1, v150, v151
	v_max3_f32 v1, v1, v152, v153
	v_max3_f32 v1, v1, v154, v155
	v_max3_f32 v1, v1, v156, v157
	v_max3_f32 v1, v1, v158, v159
	v_cmp_ge_f32_e32 vcc, s53, v1
	s_cmp_eq_u64 vcc, exec
	s_waitcnt lgkmcnt(0)
	v_mfma_scale_f32_32x32x64_f8f6f4 v[16:31], v[168:175], v[112:119], v[16:31], v207, v207 op_sel_hi:[0,0,0]
	v_mfma_scale_f32_16x16x128_f8f6f4 v[248:251], v[240:247], v[112:119], v[248:251], v207, v207 op_sel_hi:[0,0,0]
	s_cbranch_scc0 .LBB0_444
.LBB0_433:
	s_waitcnt vmcnt(4)
	s_waitcnt lgkmcnt(0)
	s_barrier
	v_mfma_scale_f32_32x32x64_f8f6f4 v[112:127], v[160:167], v[192:199], v[96:111], v207, v218 op_sel_hi:[0,0,0]
	ds_read_b128 v[184:187], v221 offset:30720
	ds_read_b128 v[228:231], v222 offset:32768
	ds_read_b128 v[224:227], v221 offset:32768
	ds_read_b128 v[176:179], v221 offset:34816
	ds_read_b128 v[188:191], v222 offset:30720
	ds_read_b128 v[180:183], v222 offset:34816
	v_cvt_pknorm_u16_f32 v1, v128, v129
	v_cvt_pknorm_u16_f32 v10, v130, v131
	v_perm_b32 v128, v10, v1, s55
	v_cvt_pknorm_u16_f32 v1, v132, v133
	v_cvt_pknorm_u16_f32 v10, v134, v135
	v_perm_b32 v129, v10, v1, s55
	v_cvt_pknorm_u16_f32 v1, v136, v137
	v_cvt_pknorm_u16_f32 v10, v138, v139
	v_perm_b32 v130, v10, v1, s55
	v_cvt_pknorm_u16_f32 v1, v140, v141
	v_cvt_pknorm_u16_f32 v10, v142, v143
	v_perm_b32 v131, v10, v1, s55
	v_mfma_scale_f32_32x32x64_f8f6f4 v[160:175], v[2:9], v[192:199], v[96:111], v207, v218 op_sel_hi:[0,0,0]
	s_add_i32 s14, s33, -2
	s_min_u32 s14, s14, s17
	s_lshl_b32 s20, s14, 13
	v_cvt_pknorm_u16_f32 v1, v144, v145
	v_cvt_pknorm_u16_f32 v2, v146, v147
	s_add_u32 s14, s4, s20
	v_perm_b32 v132, v2, v1, s55
	v_cvt_pknorm_u16_f32 v1, v148, v149
	v_cvt_pknorm_u16_f32 v2, v150, v151
	s_addc_u32 s15, s5, 0
	v_perm_b32 v133, v2, v1, s55
	v_cvt_pknorm_u16_f32 v1, v152, v153
	v_cvt_pknorm_u16_f32 v2, v154, v155
	s_add_u32 s20, s6, s20
	v_perm_b32 v134, v2, v1, s55
	v_cvt_pknorm_u16_f32 v1, v156, v157
	v_cvt_pknorm_u16_f32 v2, v158, v159
	s_addc_u32 s21, s7, 0
	v_perm_b32 v135, v2, v1, s55
	s_mov_b32 m0, s49
	v_lshl_add_u64 v[2:3], s[14:15], 0, v[200:201]
	global_load_lds_dwordx4 v[2:3], off
	v_lshl_add_u64 v[2:3], s[20:21], 0, v[202:203]
	s_mov_b32 m0, s3
	s_nop 0
	global_load_lds_dwordx4 v[2:3], off
	s_waitcnt lgkmcnt(0)
	v_mfma_scale_f32_32x32x64_f8f6f4 v[64:79], v[184:191], v[128:135], v[64:79], v207, v207 op_sel_hi:[0,0,0]
	ds_read_b128 v[136:139], v221 offset:36864
	ds_read_b128 v[140:143], v222 offset:36864
	v_mfma_scale_f32_32x32x64_f8f6f4 v[48:63], v[224:231], v[128:135], v[48:63], v207, v207 op_sel_hi:[0,0,0]
	ds_read_b128 v[144:147], v219 offset:40960
	ds_read_b128 v[2:5], v219 offset:45056
	ds_read_b128 v[148:151], v220 offset:40960
	ds_read_b128 v[6:9], v220 offset:45056
	v_mov_b32_e32 v1, v112
	v_max3_f32 v1, v1, v112, v113
	v_max3_f32 v1, v1, v114, v115
	v_max3_f32 v1, v1, v116, v117
	v_max3_f32 v1, v1, v118, v119
	v_max3_f32 v1, v1, v120, v121
	v_max3_f32 v1, v1, v122, v123
	v_max3_f32 v1, v1, v124, v125
	v_max3_f32 v1, v1, v126, v127
	v_mfma_scale_f32_32x32x64_f8f6f4 v[32:47], v[176:183], v[128:135], v[32:47], v207, v207 op_sel_hi:[0,0,0]
	v_max3_f32 v1, v1, v160, v161
	v_max3_f32 v1, v1, v162, v163
	v_max3_f32 v1, v1, v164, v165
	v_max3_f32 v1, v1, v166, v167
	v_max3_f32 v1, v1, v168, v169
	v_max3_f32 v1, v1, v170, v171
	v_max3_f32 v1, v1, v172, v173
	v_max3_f32 v1, v1, v174, v175
	v_cmp_ge_f32_e32 vcc, s53, v1
	s_cmp_eq_u64 vcc, exec
	s_waitcnt lgkmcnt(0)
	v_mfma_scale_f32_32x32x64_f8f6f4 v[16:31], v[136:143], v[128:135], v[16:31], v207, v207 op_sel_hi:[0,0,0]
	v_mfma_scale_f32_16x16x128_f8f6f4 v[248:251], v[240:247], v[128:135], v[248:251], v207, v207 op_sel_hi:[0,0,0]
	s_cbranch_scc0 .LBB0_447
.LBB0_434:
	s_waitcnt vmcnt(4)
	s_waitcnt lgkmcnt(0)
	s_barrier
	v_mfma_scale_f32_32x32x64_f8f6f4 v[128:143], v[144:151], v[192:199], v[96:111], v207, v218 op_sel_hi:[0,0,0]
	ds_read_b128 v[184:187], v221 offset:40960
	ds_read_b128 v[224:227], v221 offset:43008
	ds_read_b128 v[188:191], v222 offset:40960
	ds_read_b128 v[176:179], v221 offset:45056
	ds_read_b128 v[228:231], v222 offset:43008
	ds_read_b128 v[180:183], v222 offset:45056
	v_cvt_pknorm_u16_f32 v1, v112, v113
	v_cvt_pknorm_u16_f32 v10, v114, v115
	v_perm_b32 v112, v10, v1, s55
	v_cvt_pknorm_u16_f32 v1, v116, v117
	v_cvt_pknorm_u16_f32 v10, v118, v119
	v_perm_b32 v113, v10, v1, s55
	v_cvt_pknorm_u16_f32 v1, v120, v121
	v_cvt_pknorm_u16_f32 v10, v122, v123
	v_perm_b32 v114, v10, v1, s55
	v_cvt_pknorm_u16_f32 v1, v124, v125
	v_cvt_pknorm_u16_f32 v10, v126, v127
	v_perm_b32 v115, v10, v1, s55
	v_mfma_scale_f32_32x32x64_f8f6f4 v[144:159], v[2:9], v[192:199], v[96:111], v207, v218 op_sel_hi:[0,0,0]
	s_add_i32 s14, s33, -1
	s_min_u32 s14, s14, s17
	s_lshl_b32 s20, s14, 13
	v_cvt_pknorm_u16_f32 v1, v160, v161
	v_cvt_pknorm_u16_f32 v2, v162, v163
	s_add_u32 s14, s4, s20
	v_perm_b32 v116, v2, v1, s55
	v_cvt_pknorm_u16_f32 v1, v164, v165
	v_cvt_pknorm_u16_f32 v2, v166, v167
	s_addc_u32 s15, s5, 0
	v_perm_b32 v117, v2, v1, s55
	v_cvt_pknorm_u16_f32 v1, v168, v169
	v_cvt_pknorm_u16_f32 v2, v170, v171
	s_add_u32 s20, s6, s20
	v_perm_b32 v118, v2, v1, s55
	v_cvt_pknorm_u16_f32 v1, v172, v173
	v_cvt_pknorm_u16_f32 v2, v174, v175
	s_addc_u32 s21, s7, 0
	v_perm_b32 v119, v2, v1, s55
	s_mov_b32 m0, s50
	v_lshl_add_u64 v[2:3], s[14:15], 0, v[200:201]
	global_load_lds_dwordx4 v[2:3], off
	v_lshl_add_u64 v[2:3], s[20:21], 0, v[202:203]
	s_mov_b32 m0, s27
	s_nop 0
	global_load_lds_dwordx4 v[2:3], off
	s_waitcnt lgkmcnt(0)
	v_mfma_scale_f32_32x32x64_f8f6f4 v[64:79], v[184:191], v[112:119], v[64:79], v207, v207 op_sel_hi:[0,0,0]
	ds_read_b128 v[120:123], v221 offset:47104
	ds_read_b128 v[124:127], v222 offset:47104
	v_mfma_scale_f32_32x32x64_f8f6f4 v[48:63], v[224:231], v[112:119], v[48:63], v207, v207 op_sel_hi:[0,0,0]
	ds_read_b128 v[160:163], v219
	ds_read_b128 v[2:5], v219 offset:4096
	ds_read_b128 v[164:167], v220
	ds_read_b128 v[6:9], v220 offset:4096
	v_mov_b32_e32 v1, v128
	v_max3_f32 v1, v1, v128, v129
	v_max3_f32 v1, v1, v130, v131
	v_max3_f32 v1, v1, v132, v133
	v_max3_f32 v1, v1, v134, v135
	v_max3_f32 v1, v1, v136, v137
	v_max3_f32 v1, v1, v138, v139
	v_max3_f32 v1, v1, v140, v141
	v_max3_f32 v1, v1, v142, v143
	v_mfma_scale_f32_32x32x64_f8f6f4 v[32:47], v[176:183], v[112:119], v[32:47], v207, v207 op_sel_hi:[0,0,0]
	v_max3_f32 v1, v1, v144, v145
	v_max3_f32 v1, v1, v146, v147
	v_max3_f32 v1, v1, v148, v149
	v_max3_f32 v1, v1, v150, v151
	v_max3_f32 v1, v1, v152, v153
	v_max3_f32 v1, v1, v154, v155
	v_max3_f32 v1, v1, v156, v157
	v_max3_f32 v1, v1, v158, v159
	v_cmp_ge_f32_e32 vcc, s53, v1
	s_cmp_eq_u64 vcc, exec
	s_waitcnt lgkmcnt(0)
	v_mfma_scale_f32_32x32x64_f8f6f4 v[16:31], v[120:127], v[112:119], v[16:31], v207, v207 op_sel_hi:[0,0,0]
	v_mfma_scale_f32_16x16x128_f8f6f4 v[248:251], v[240:247], v[112:119], v[248:251], v207, v207 op_sel_hi:[0,0,0]
	s_cbranch_scc0 .LBB0_450
.LBB0_435:
	s_waitcnt vmcnt(4)
	s_waitcnt lgkmcnt(0)
	s_barrier
	v_mfma_scale_f32_32x32x64_f8f6f4 v[112:127], v[160:167], v[192:199], v[96:111], v207, v218 op_sel_hi:[0,0,0]
	ds_read_b128 v[176:179], v221 offset:51200
	ds_read_b128 v[184:187], v221 offset:53248
	ds_read_b128 v[180:183], v222 offset:51200
	ds_read_b128 v[168:171], v221 offset:55296
	ds_read_b128 v[188:191], v222 offset:53248
	ds_read_b128 v[172:175], v222 offset:55296
	v_cvt_pknorm_u16_f32 v1, v128, v129
	v_cvt_pknorm_u16_f32 v10, v130, v131
	v_perm_b32 v160, v10, v1, s55
	v_cvt_pknorm_u16_f32 v1, v132, v133
	v_cvt_pknorm_u16_f32 v10, v134, v135
	v_perm_b32 v161, v10, v1, s55
	v_cvt_pknorm_u16_f32 v1, v136, v137
	v_cvt_pknorm_u16_f32 v10, v138, v139
	v_perm_b32 v162, v10, v1, s55
	v_cvt_pknorm_u16_f32 v1, v140, v141
	v_cvt_pknorm_u16_f32 v10, v142, v143
	v_perm_b32 v163, v10, v1, s55
	v_mfma_scale_f32_32x32x64_f8f6f4 v[128:143], v[2:9], v[192:199], v[96:111], v207, v218 op_sel_hi:[0,0,0]
	s_min_u32 s14, s33, s17
	s_lshl_b32 s20, s14, 13
	v_cvt_pknorm_u16_f32 v1, v144, v145
	v_cvt_pknorm_u16_f32 v2, v146, v147
	s_add_u32 s14, s4, s20
	v_perm_b32 v164, v2, v1, s55
	v_cvt_pknorm_u16_f32 v1, v148, v149
	v_cvt_pknorm_u16_f32 v2, v150, v151
	s_addc_u32 s15, s5, 0
	v_perm_b32 v165, v2, v1, s55
	v_cvt_pknorm_u16_f32 v1, v152, v153
	v_cvt_pknorm_u16_f32 v2, v154, v155
	s_add_u32 s20, s6, s20
	v_perm_b32 v166, v2, v1, s55
	v_cvt_pknorm_u16_f32 v1, v156, v157
	v_cvt_pknorm_u16_f32 v2, v158, v159
	s_addc_u32 s21, s7, 0
	v_perm_b32 v167, v2, v1, s55
	s_mov_b32 m0, s51
	v_lshl_add_u64 v[2:3], s[14:15], 0, v[200:201]
	global_load_lds_dwordx4 v[2:3], off
	v_lshl_add_u64 v[2:3], s[20:21], 0, v[202:203]
	s_mov_b32 m0, s26
	s_nop 0
	global_load_lds_dwordx4 v[2:3], off
	s_waitcnt lgkmcnt(0)
	v_mfma_scale_f32_32x32x64_f8f6f4 v[64:79], v[176:183], v[160:167], v[64:79], v207, v207 op_sel_hi:[0,0,0]
	ds_read_b128 v[2:5], v221 offset:57344
	ds_read_b128 v[6:9], v222 offset:57344
	v_mfma_scale_f32_32x32x64_f8f6f4 v[48:63], v[184:191], v[160:167], v[48:63], v207, v207 op_sel_hi:[0,0,0]
	ds_read_b128 v[184:187], v219 offset:8192
	ds_read_b128 v[176:179], v219 offset:12288
	ds_read_b128 v[188:191], v220 offset:8192
	ds_read_b128 v[180:183], v220 offset:12288
	v_mov_b32_e32 v1, v112
	v_max3_f32 v1, v1, v112, v113
	v_max3_f32 v1, v1, v114, v115
	v_max3_f32 v1, v1, v116, v117
	v_max3_f32 v1, v1, v118, v119
	v_max3_f32 v1, v1, v120, v121
	v_max3_f32 v1, v1, v122, v123
	v_max3_f32 v1, v1, v124, v125
	v_max3_f32 v1, v1, v126, v127
	v_mfma_scale_f32_32x32x64_f8f6f4 v[32:47], v[168:175], v[160:167], v[32:47], v207, v207 op_sel_hi:[0,0,0]
	v_max3_f32 v1, v1, v128, v129
	v_max3_f32 v1, v1, v130, v131
	v_max3_f32 v1, v1, v132, v133
	v_max3_f32 v1, v1, v134, v135
	v_max3_f32 v1, v1, v136, v137
	v_max3_f32 v1, v1, v138, v139
	v_max3_f32 v1, v1, v140, v141
	v_max3_f32 v1, v1, v142, v143
	v_cmp_ge_f32_e32 vcc, s53, v1
	s_cmp_eq_u64 vcc, exec
	s_waitcnt lgkmcnt(0)
	v_mfma_scale_f32_32x32x64_f8f6f4 v[16:31], v[2:9], v[160:167], v[16:31], v207, v207 op_sel_hi:[0,0,0]
	v_mfma_scale_f32_16x16x128_f8f6f4 v[248:251], v[240:247], v[160:167], v[248:251], v207, v207 op_sel_hi:[0,0,0]
	s_cbranch_scc0 .LBB0_453

.LBB0_440:
	s_nop 15
	s_nop 15
	s_nop 0
	v_pk_mul_f32 v[78:79], v[10:11], v[78:79] op_sel_hi:[0,1]
	v_pk_mul_f32 v[76:77], v[10:11], v[76:77] op_sel_hi:[0,1]
	v_pk_mul_f32 v[74:75], v[10:11], v[74:75] op_sel_hi:[0,1]
	v_pk_mul_f32 v[72:73], v[10:11], v[72:73] op_sel_hi:[0,1]
	v_pk_mul_f32 v[70:71], v[10:11], v[70:71] op_sel_hi:[0,1]
	v_pk_mul_f32 v[68:69], v[10:11], v[68:69] op_sel_hi:[0,1]
	v_pk_mul_f32 v[66:67], v[10:11], v[66:67] op_sel_hi:[0,1]
	v_pk_mul_f32 v[64:65], v[10:11], v[64:65] op_sel_hi:[0,1]
	v_pk_mul_f32 v[62:63], v[10:11], v[62:63] op_sel_hi:[0,1]
	v_pk_mul_f32 v[60:61], v[10:11], v[60:61] op_sel_hi:[0,1]
	v_pk_mul_f32 v[58:59], v[10:11], v[58:59] op_sel_hi:[0,1]
	v_pk_mul_f32 v[56:57], v[10:11], v[56:57] op_sel_hi:[0,1]
	v_pk_mul_f32 v[54:55], v[10:11], v[54:55] op_sel_hi:[0,1]
	v_pk_mul_f32 v[52:53], v[10:11], v[52:53] op_sel_hi:[0,1]
	v_pk_mul_f32 v[50:51], v[10:11], v[50:51] op_sel_hi:[0,1]
	v_pk_mul_f32 v[48:49], v[10:11], v[48:49] op_sel_hi:[0,1]
	v_pk_mul_f32 v[46:47], v[10:11], v[46:47] op_sel_hi:[0,1]
	v_pk_mul_f32 v[44:45], v[10:11], v[44:45] op_sel_hi:[0,1]
	v_pk_mul_f32 v[42:43], v[10:11], v[42:43] op_sel_hi:[0,1]
	v_pk_mul_f32 v[40:41], v[10:11], v[40:41] op_sel_hi:[0,1]
	v_pk_mul_f32 v[38:39], v[10:11], v[38:39] op_sel_hi:[0,1]
	v_pk_mul_f32 v[36:37], v[10:11], v[36:37] op_sel_hi:[0,1]
	v_pk_mul_f32 v[34:35], v[10:11], v[34:35] op_sel_hi:[0,1]
	v_pk_mul_f32 v[32:33], v[10:11], v[32:33] op_sel_hi:[0,1]
	v_pk_mul_f32 v[30:31], v[10:11], v[30:31] op_sel_hi:[0,1]
	v_pk_mul_f32 v[28:29], v[10:11], v[28:29] op_sel_hi:[0,1]
	v_pk_mul_f32 v[26:27], v[10:11], v[26:27] op_sel_hi:[0,1]
	v_pk_mul_f32 v[24:25], v[10:11], v[24:25] op_sel_hi:[0,1]
	v_pk_mul_f32 v[22:23], v[10:11], v[22:23] op_sel_hi:[0,1]
	v_pk_mul_f32 v[20:21], v[10:11], v[20:21] op_sel_hi:[0,1]
	v_pk_mul_f32 v[18:19], v[10:11], v[18:19] op_sel_hi:[0,1]
	v_pk_mul_f32 v[16:17], v[10:11], v[16:17] op_sel_hi:[0,1]
	v_pk_mul_f32 v[94:95], v[10:11], v[94:95] op_sel_hi:[0,1]
	v_pk_mul_f32 v[92:93], v[10:11], v[92:93] op_sel_hi:[0,1]
	v_pk_mul_f32 v[90:91], v[10:11], v[90:91] op_sel_hi:[0,1]
	v_pk_mul_f32 v[88:89], v[10:11], v[88:89] op_sel_hi:[0,1]
	v_pk_mul_f32 v[86:87], v[10:11], v[86:87] op_sel_hi:[0,1]
	v_pk_mul_f32 v[84:85], v[10:11], v[84:85] op_sel_hi:[0,1]
	v_pk_mul_f32 v[82:83], v[10:11], v[82:83] op_sel_hi:[0,1]
	v_pk_mul_f32 v[80:81], v[10:11], v[80:81] op_sel_hi:[0,1]
	v_mov_b32_e32 v252, v10
	v_mov_b32_e32 v253, v10
	s_nop 1
	v_permlane16_swap_b32_e32 v252, v253
	v_mul_f32_e32 v248, v248, v10
	s_nop 0
	v_mul_f32_e32 v249, v249, v253
	s_branch .LBB0_431

.LBB0_455:
	s_nop 15
	s_nop 15
	s_nop 0
	v_pk_mul_f32 v[78:79], v[2:3], v[78:79] op_sel_hi:[0,1]
	v_pk_mul_f32 v[76:77], v[2:3], v[76:77] op_sel_hi:[0,1]
	v_pk_mul_f32 v[74:75], v[2:3], v[74:75] op_sel_hi:[0,1]
	v_pk_mul_f32 v[72:73], v[2:3], v[72:73] op_sel_hi:[0,1]
	v_pk_mul_f32 v[70:71], v[2:3], v[70:71] op_sel_hi:[0,1]
	v_pk_mul_f32 v[68:69], v[2:3], v[68:69] op_sel_hi:[0,1]
	v_pk_mul_f32 v[66:67], v[2:3], v[66:67] op_sel_hi:[0,1]
	v_pk_mul_f32 v[64:65], v[2:3], v[64:65] op_sel_hi:[0,1]
	v_pk_mul_f32 v[62:63], v[2:3], v[62:63] op_sel_hi:[0,1]
	v_pk_mul_f32 v[60:61], v[2:3], v[60:61] op_sel_hi:[0,1]
	v_pk_mul_f32 v[58:59], v[2:3], v[58:59] op_sel_hi:[0,1]
	v_pk_mul_f32 v[56:57], v[2:3], v[56:57] op_sel_hi:[0,1]
	v_pk_mul_f32 v[54:55], v[2:3], v[54:55] op_sel_hi:[0,1]
	v_pk_mul_f32 v[52:53], v[2:3], v[52:53] op_sel_hi:[0,1]
	v_pk_mul_f32 v[50:51], v[2:3], v[50:51] op_sel_hi:[0,1]
	v_pk_mul_f32 v[48:49], v[2:3], v[48:49] op_sel_hi:[0,1]
	v_pk_mul_f32 v[46:47], v[2:3], v[46:47] op_sel_hi:[0,1]
	v_pk_mul_f32 v[44:45], v[2:3], v[44:45] op_sel_hi:[0,1]
	v_pk_mul_f32 v[42:43], v[2:3], v[42:43] op_sel_hi:[0,1]
	v_pk_mul_f32 v[40:41], v[2:3], v[40:41] op_sel_hi:[0,1]
	v_pk_mul_f32 v[38:39], v[2:3], v[38:39] op_sel_hi:[0,1]
	v_pk_mul_f32 v[36:37], v[2:3], v[36:37] op_sel_hi:[0,1]
	v_pk_mul_f32 v[34:35], v[2:3], v[34:35] op_sel_hi:[0,1]
	v_pk_mul_f32 v[32:33], v[2:3], v[32:33] op_sel_hi:[0,1]
	v_pk_mul_f32 v[30:31], v[2:3], v[30:31] op_sel_hi:[0,1]
	v_pk_mul_f32 v[28:29], v[2:3], v[28:29] op_sel_hi:[0,1]
	v_pk_mul_f32 v[26:27], v[2:3], v[26:27] op_sel_hi:[0,1]
	v_pk_mul_f32 v[24:25], v[2:3], v[24:25] op_sel_hi:[0,1]
	v_pk_mul_f32 v[22:23], v[2:3], v[22:23] op_sel_hi:[0,1]
	v_pk_mul_f32 v[20:21], v[2:3], v[20:21] op_sel_hi:[0,1]
	v_pk_mul_f32 v[18:19], v[2:3], v[18:19] op_sel_hi:[0,1]
	v_pk_mul_f32 v[16:17], v[2:3], v[16:17] op_sel_hi:[0,1]
	v_pk_mul_f32 v[94:95], v[2:3], v[94:95] op_sel_hi:[0,1]
	v_pk_mul_f32 v[92:93], v[2:3], v[92:93] op_sel_hi:[0,1]
	v_pk_mul_f32 v[90:91], v[2:3], v[90:91] op_sel_hi:[0,1]
	v_pk_mul_f32 v[88:89], v[2:3], v[88:89] op_sel_hi:[0,1]
	v_pk_mul_f32 v[86:87], v[2:3], v[86:87] op_sel_hi:[0,1]
	v_pk_mul_f32 v[84:85], v[2:3], v[84:85] op_sel_hi:[0,1]
	v_pk_mul_f32 v[82:83], v[2:3], v[82:83] op_sel_hi:[0,1]
	v_pk_mul_f32 v[80:81], v[2:3], v[80:81] op_sel_hi:[0,1]
	v_mov_b32_e32 v252, v2
	v_mov_b32_e32 v253, v2
	s_nop 1
	v_permlane16_swap_b32_e32 v252, v253
	v_mul_f32_e32 v248, v248, v2
	s_nop 0
	v_mul_f32_e32 v249, v249, v253
	s_branch .LBB0_436

.LBB0_479:
	s_nop 15
	s_nop 15
	s_nop 0
	v_pk_mul_f32 v[78:79], v[2:3], v[78:79] op_sel_hi:[0,1]
	v_pk_mul_f32 v[76:77], v[2:3], v[76:77] op_sel_hi:[0,1]
	v_pk_mul_f32 v[74:75], v[2:3], v[74:75] op_sel_hi:[0,1]
	v_pk_mul_f32 v[72:73], v[2:3], v[72:73] op_sel_hi:[0,1]
	v_pk_mul_f32 v[70:71], v[2:3], v[70:71] op_sel_hi:[0,1]
	v_pk_mul_f32 v[68:69], v[2:3], v[68:69] op_sel_hi:[0,1]
	v_pk_mul_f32 v[66:67], v[2:3], v[66:67] op_sel_hi:[0,1]
	v_pk_mul_f32 v[64:65], v[2:3], v[64:65] op_sel_hi:[0,1]
	v_pk_mul_f32 v[62:63], v[2:3], v[62:63] op_sel_hi:[0,1]
	v_pk_mul_f32 v[60:61], v[2:3], v[60:61] op_sel_hi:[0,1]
	v_pk_mul_f32 v[58:59], v[2:3], v[58:59] op_sel_hi:[0,1]
	v_pk_mul_f32 v[56:57], v[2:3], v[56:57] op_sel_hi:[0,1]
	v_pk_mul_f32 v[54:55], v[2:3], v[54:55] op_sel_hi:[0,1]
	v_pk_mul_f32 v[52:53], v[2:3], v[52:53] op_sel_hi:[0,1]
	v_pk_mul_f32 v[50:51], v[2:3], v[50:51] op_sel_hi:[0,1]
	v_pk_mul_f32 v[48:49], v[2:3], v[48:49] op_sel_hi:[0,1]
	v_pk_mul_f32 v[46:47], v[2:3], v[46:47] op_sel_hi:[0,1]
	v_pk_mul_f32 v[44:45], v[2:3], v[44:45] op_sel_hi:[0,1]
	v_pk_mul_f32 v[42:43], v[2:3], v[42:43] op_sel_hi:[0,1]
	v_pk_mul_f32 v[40:41], v[2:3], v[40:41] op_sel_hi:[0,1]
	v_pk_mul_f32 v[38:39], v[2:3], v[38:39] op_sel_hi:[0,1]
	v_pk_mul_f32 v[36:37], v[2:3], v[36:37] op_sel_hi:[0,1]
	v_pk_mul_f32 v[34:35], v[2:3], v[34:35] op_sel_hi:[0,1]
	v_pk_mul_f32 v[32:33], v[2:3], v[32:33] op_sel_hi:[0,1]
	v_pk_mul_f32 v[30:31], v[2:3], v[30:31] op_sel_hi:[0,1]
	v_pk_mul_f32 v[28:29], v[2:3], v[28:29] op_sel_hi:[0,1]
	v_pk_mul_f32 v[26:27], v[2:3], v[26:27] op_sel_hi:[0,1]
	v_pk_mul_f32 v[24:25], v[2:3], v[24:25] op_sel_hi:[0,1]
	v_pk_mul_f32 v[22:23], v[2:3], v[22:23] op_sel_hi:[0,1]
	v_pk_mul_f32 v[20:21], v[2:3], v[20:21] op_sel_hi:[0,1]
	v_pk_mul_f32 v[18:19], v[2:3], v[18:19] op_sel_hi:[0,1]
	v_pk_mul_f32 v[16:17], v[2:3], v[16:17] op_sel_hi:[0,1]
	v_pk_mul_f32 v[94:95], v[2:3], v[94:95] op_sel_hi:[0,1]
	v_pk_mul_f32 v[92:93], v[2:3], v[92:93] op_sel_hi:[0,1]
	v_pk_mul_f32 v[90:91], v[2:3], v[90:91] op_sel_hi:[0,1]
	v_pk_mul_f32 v[88:89], v[2:3], v[88:89] op_sel_hi:[0,1]
	v_pk_mul_f32 v[86:87], v[2:3], v[86:87] op_sel_hi:[0,1]
	v_pk_mul_f32 v[84:85], v[2:3], v[84:85] op_sel_hi:[0,1]
	v_pk_mul_f32 v[82:83], v[2:3], v[82:83] op_sel_hi:[0,1]
	v_pk_mul_f32 v[80:81], v[2:3], v[80:81] op_sel_hi:[0,1]
	v_mov_b32_e32 v252, v2
	v_mov_b32_e32 v253, v2
	s_nop 1
	v_permlane16_swap_b32_e32 v252, v253
	v_mul_f32_e32 v248, v248, v2
	s_nop 0
	v_mul_f32_e32 v249, v249, v253
.LBB0_480:
	v_cvt_pknorm_u16_f32 v1, v160, v161
	v_cvt_pknorm_u16_f32 v2, v162, v163
	v_perm_b32 v2, v2, v1, s55
	v_cvt_pknorm_u16_f32 v1, v144, v145
	v_cvt_pknorm_u16_f32 v3, v146, v147
	v_perm_b32 v6, v3, v1, s55
	v_cvt_pknorm_u16_f32 v1, v164, v165
	v_cvt_pknorm_u16_f32 v3, v166, v167
	v_perm_b32 v3, v3, v1, s55
	v_cvt_pknorm_u16_f32 v1, v148, v149
	v_cvt_pknorm_u16_f32 v4, v150, v151
	v_perm_b32 v7, v4, v1, s55
	v_cvt_pknorm_u16_f32 v1, v168, v169
	v_cvt_pknorm_u16_f32 v4, v170, v171
	s_mul_hi_u32 s2, s17, 0xaaaaaaab
	v_perm_b32 v4, v4, v1, s55
	v_cvt_pknorm_u16_f32 v1, v152, v153
	v_cvt_pknorm_u16_f32 v5, v154, v155
	s_lshr_b32 s2, s2, 2
	v_perm_b32 v8, v5, v1, s55
	v_cvt_pknorm_u16_f32 v1, v172, v173
	v_cvt_pknorm_u16_f32 v5, v174, v175
	s_mul_i32 s2, s2, 6
	v_perm_b32 v5, v5, v1, s55
	v_cvt_pknorm_u16_f32 v1, v156, v157
	v_cvt_pknorm_u16_f32 v9, v158, v159
	s_sub_i32 s2, s17, s2
	v_perm_b32 v9, v9, v1, s55
	s_mulk_i32 s2, 0x2800
	s_add_i32 s2, s10, s2
	v_add_u32_e32 v1, s2, v208
	s_nop 4
	v_add_u32_e32 v10, v1, v209
	v_add_u32_e32 v1, v1, v217
	ds_read_b128 v[96:99], v10
	ds_read_b128 v[100:103], v1
	s_mov_b32 s2, s47
	s_waitcnt lgkmcnt(0)
	v_mfma_scale_f32_32x32x64_f8f6f4 v[64:79], v[96:103], v[2:9], v[64:79], v207, v207 op_sel_hi:[0,0,0]
	ds_read_b128 v[96:99], v10 offset:2048
	ds_read_b128 v[100:103], v1 offset:2048
	s_waitcnt lgkmcnt(0)
	v_mfma_scale_f32_32x32x64_f8f6f4 v[48:63], v[96:103], v[2:9], v[48:63], v207, v207 op_sel_hi:[0,0,0]
	ds_read_b128 v[96:99], v10 offset:4096
	ds_read_b128 v[100:103], v1 offset:4096
	s_waitcnt lgkmcnt(0)
	v_mfma_scale_f32_32x32x64_f8f6f4 v[32:47], v[96:103], v[2:9], v[32:47], v207, v207 op_sel_hi:[0,0,0]
	ds_read_b128 v[96:99], v10 offset:6144
	ds_read_b128 v[100:103], v1 offset:6144
	s_waitcnt lgkmcnt(0)
	v_mfma_scale_f32_32x32x64_f8f6f4 v[16:31], v[96:103], v[2:9], v[16:31], v207, v207 op_sel_hi:[0,0,0]
	ds_read_b128 v[96:99], v10 offset:8192
	ds_read_b128 v[100:103], v1 offset:8192
	s_waitcnt lgkmcnt(0)
	v_mfma_scale_f32_32x32x64_f8f6f4 v[80:95], v[96:103], v[2:9], v[80:95], v207, v207 op_sel_hi:[0,0,0]
	s_nop 0
	s_nop 15
	s_nop 15
	v_mbcnt_lo_u32_b32 v2, -1, 0
	v_mbcnt_hi_u32_b32 v2, -1, v2
	s_waitcnt vmcnt(0)
	s_waitcnt vmcnt(0)
	v_lshl_add_u32 v3, s2, 6, v2
	v_and_b32_e32 v252, 15, v2
	v_lshlrev_b32_e32 v252, 2, v252
	ds_bpermute_b32 v253, v252, v248
	ds_bpermute_b32 v254, v252, v249
	v_and_b32_e32 v1, 16, v2
	v_cmp_ne_u32_e32 vcc, 0, v1
	s_waitcnt lgkmcnt(0)
	s_nop 0
	v_cndmask_b32_e32 v253, v253, v254, vcc
	v_add_f32_e32 v80, v80, v253
	v_rcp_f32_e32 v1, v80
	v_lshlrev_b32_e32 v5, 8, v3
	v_and_b32_e32 v5, 0xc000, v5
	v_and_b32_e32 v4, 63, v2
	v_add_u32_e32 v5, s10, v5
	v_and_b32_e32 v6, 0xffffff00, v3
	v_cmp_eq_u32_e32 vcc, s71, v6
	v_lshl_add_u32 v14, v4, 2, v5
	s_barrier
	s_and_saveexec_b64 s[4:5], vcc
	s_cbranch_execz .LBB0_482
	v_mul_f32_e32 v4, v206, v1
	v_mul_f32_e32 v5, v64, v4
	v_mul_f32_e32 v6, v65, v4
	ds_write2st64_b32 v14, v5, v6 offset1:1
	v_mul_f32_e32 v5, v66, v4
	v_mul_f32_e32 v6, v67, v4
	ds_write2st64_b32 v14, v5, v6 offset0:2 offset1:3
	v_mul_f32_e32 v5, v68, v4
	v_mul_f32_e32 v6, v69, v4
	ds_write2st64_b32 v14, v5, v6 offset0:4 offset1:5
	v_mul_f32_e32 v5, v70, v4
	v_mul_f32_e32 v6, v71, v4
	ds_write2st64_b32 v14, v5, v6 offset0:6 offset1:7
	v_mul_f32_e32 v5, v72, v4
	v_mul_f32_e32 v6, v73, v4
	ds_write2st64_b32 v14, v5, v6 offset0:8 offset1:9
	v_mul_f32_e32 v5, v74, v4
	v_mul_f32_e32 v6, v75, v4
	ds_write2st64_b32 v14, v5, v6 offset0:10 offset1:11
	v_mul_f32_e32 v5, v76, v4
	v_mul_f32_e32 v6, v77, v4
	ds_write2st64_b32 v14, v5, v6 offset0:12 offset1:13
	v_mul_f32_e32 v5, v78, v4
	v_mul_f32_e32 v6, v79, v4
	ds_write2st64_b32 v14, v5, v6 offset0:14 offset1:15
	v_mul_f32_e32 v5, v48, v4
	v_mul_f32_e32 v6, v49, v4
	ds_write2st64_b32 v14, v5, v6 offset0:16 offset1:17
	v_mul_f32_e32 v5, v50, v4
	v_mul_f32_e32 v6, v51, v4
	ds_write2st64_b32 v14, v5, v6 offset0:18 offset1:19
	v_mul_f32_e32 v5, v52, v4
	v_mul_f32_e32 v6, v53, v4
	ds_write2st64_b32 v14, v5, v6 offset0:20 offset1:21
	v_mul_f32_e32 v5, v54, v4
	v_mul_f32_e32 v6, v55, v4
	ds_write2st64_b32 v14, v5, v6 offset0:22 offset1:23
	v_mul_f32_e32 v5, v56, v4
	v_mul_f32_e32 v6, v57, v4
	ds_write2st64_b32 v14, v5, v6 offset0:24 offset1:25
	v_mul_f32_e32 v5, v58, v4
	v_mul_f32_e32 v6, v59, v4
	ds_write2st64_b32 v14, v5, v6 offset0:26 offset1:27
	v_mul_f32_e32 v5, v60, v4
	v_mul_f32_e32 v6, v61, v4
	ds_write2st64_b32 v14, v5, v6 offset0:28 offset1:29
	v_mul_f32_e32 v5, v62, v4
	v_mul_f32_e32 v6, v63, v4
	ds_write2st64_b32 v14, v5, v6 offset0:30 offset1:31
	v_mul_f32_e32 v5, v32, v4
	v_mul_f32_e32 v6, v33, v4
	ds_write2st64_b32 v14, v5, v6 offset0:32 offset1:33
	v_mul_f32_e32 v5, v34, v4
	v_mul_f32_e32 v6, v35, v4
	ds_write2st64_b32 v14, v5, v6 offset0:34 offset1:35
	v_mul_f32_e32 v5, v36, v4
	v_mul_f32_e32 v6, v37, v4
	ds_write2st64_b32 v14, v5, v6 offset0:36 offset1:37
	v_mul_f32_e32 v5, v38, v4
	v_mul_f32_e32 v6, v39, v4
	ds_write2st64_b32 v14, v5, v6 offset0:38 offset1:39
	v_mul_f32_e32 v5, v40, v4
	v_mul_f32_e32 v6, v41, v4
	ds_write2st64_b32 v14, v5, v6 offset0:40 offset1:41
	v_mul_f32_e32 v5, v42, v4
	v_mul_f32_e32 v6, v43, v4
	ds_write2st64_b32 v14, v5, v6 offset0:42 offset1:43
	v_mul_f32_e32 v5, v44, v4
	v_mul_f32_e32 v6, v45, v4
	ds_write2st64_b32 v14, v5, v6 offset0:44 offset1:45
	v_mul_f32_e32 v5, v46, v4
	v_mul_f32_e32 v6, v47, v4
	ds_write2st64_b32 v14, v5, v6 offset0:46 offset1:47
	v_mul_f32_e32 v5, v16, v4
	v_mul_f32_e32 v6, v17, v4
	ds_write2st64_b32 v14, v5, v6 offset0:48 offset1:49
	v_mul_f32_e32 v5, v18, v4
	v_mul_f32_e32 v6, v19, v4
	ds_write2st64_b32 v14, v5, v6 offset0:50 offset1:51
	v_mul_f32_e32 v5, v20, v4
	v_mul_f32_e32 v6, v21, v4
	ds_write2st64_b32 v14, v5, v6 offset0:52 offset1:53
	v_mul_f32_e32 v5, v22, v4
	v_mul_f32_e32 v6, v23, v4
	ds_write2st64_b32 v14, v5, v6 offset0:54 offset1:55
	v_mul_f32_e32 v5, v24, v4
	v_mul_f32_e32 v6, v25, v4
	ds_write2st64_b32 v14, v5, v6 offset0:56 offset1:57
	v_mul_f32_e32 v5, v26, v4
	v_mul_f32_e32 v6, v27, v4
	ds_write2st64_b32 v14, v5, v6 offset0:58 offset1:59
	v_mul_f32_e32 v5, v28, v4
	v_mul_f32_e32 v6, v29, v4
	ds_write2st64_b32 v14, v5, v6 offset0:60 offset1:61
	v_mul_f32_e32 v5, v30, v4
	v_mul_f32_e32 v4, v31, v4
	ds_write2st64_b32 v14, v5, v4 offset0:62 offset1:63
